# four-waves-per-row version with the blocks of one XCD (blockIdx mod 8) assigned adjacent rows inside the 250-row band
# baseline (speedup 1.0000x reference)
_Z11attn_kernelPKfS0_PKDv8_DF16_S0_Pfi:
	s_load_dwordx2 s[28:29], s[0:1], 0x0
	v_cmp_gt_u32_e32 vcc, 16, v0
	s_and_saveexec_b64 s[4:5], vcc
	v_lshlrev_b32_e32 v1, 2, v0
	v_mov_b32_e32 v2, 0
	ds_write_b32 v1, v2 offset:36864
	s_or_b64 exec, exec, s[4:5]
	s_load_dword s33, s[0:1], 0x28
	v_bfe_u32 v1, v0, 6, 2
	v_lshl_or_b32 v82, s2, 2, v1
	v_readfirstlane_b32 s34, v0
	s_cmp_gt_u32 s34, 0xff
	s_cbranch_scc1 .Lsc_early_skip
	v_and_b32_e32 v3, 63, v0
	v_lshlrev_b32_e32 v2, 4, v3
	s_lshr_b32 s55, s34, 6
	s_mul_i32 s43, s55, 0x2800
	s_and_b32 s56, s2, 7
	s_lshr_b32 s57, s2, 3
	s_mul_i32 s37, s56, 31
	s_min_u32 s56, s56, 2
	s_add_u32 s37, s37, s56
	s_add_u32 s37, s37, s57
	s_and_b32 s47, s37, 1
	s_lshl_b32 s47, s47, 2
	s_mul_i32 s38, s37, 0x9c40
	s_lshl_b32 s40, s47, 4
	s_sub_u32 s38, s38, s40
	s_add_u32 s38, s38, s43
	s_waitcnt lgkmcnt(0)
	s_and_b32 s29, s29, 0xffff
	s_mov_b32 s30, 0x17d78400
	s_mov_b32 s31, 0x20000
	v_mov_b32_e32 v12, v2
	v_mov_b32_e32 v4, v2
	s_cmp_lg_u32 s55, 0
	s_cbranch_scc1 .Lsc_flpa
	v_max_u32_e32 v12, s47, v3
	v_lshlrev_b32_e32 v12, 4, v12

.Lsc_early_skip:
	s_waitcnt lgkmcnt(0)
	s_barrier
	v_cmp_gt_i32_e32 vcc, s33, v82
	s_and_saveexec_b64 s[4:5], vcc
	s_cbranch_execz .LBB1_384
	s_abs_i32 s3, s33
	v_cvt_f32_u32_e32 v2, s3
	s_movk_i32 s4, 0xff
	v_sub_u32_e32 v3, 0x270f, v82
	v_cmp_lt_u32_e32 vcc, s4, v0
	v_rcp_iflag_f32_e32 v2, v2
	v_sub_u32_e32 v5, 0, v3
	s_sub_i32 s4, 0, s3
	v_xor_b32_e32 v4, s33, v3
	v_mul_f32_e32 v2, 0x4f7ffffe, v2
	v_cvt_u32_f32_e32 v2, v2
	v_max_i32_e32 v3, v3, v5
	v_ashrrev_i32_e32 v4, 31, v4
	v_mul_lo_u32 v5, s4, v2
	v_mul_hi_u32 v5, v2, v5
	v_add_u32_e32 v2, v2, v5
	v_mul_hi_u32 v2, v3, v2
	v_mul_lo_u32 v5, v2, s3
	v_sub_u32_e32 v3, v3, v5
	v_add_u32_e32 v5, 1, v2
	v_cmp_le_u32_e64 s[4:5], s3, v3
	v_and_b32_e32 v83, 63, v0
	s_nop 0
	v_cndmask_b32_e64 v2, v2, v5, s[4:5]
	v_subrev_u32_e32 v5, s3, v3
	v_cndmask_b32_e64 v3, v3, v5, s[4:5]
	v_add_u32_e32 v5, 1, v2
	v_cmp_le_u32_e64 s[4:5], s3, v3
	s_nop 1
	v_cndmask_b32_e64 v2, v2, v5, s[4:5]
	v_xor_b32_e32 v2, v2, v4
	v_sub_u32_e32 v84, v2, v4
	s_and_saveexec_b64 s[4:5], vcc
	s_xor_b64 s[30:31], exec, s[4:5]
	s_cbranch_execz .LBB1_217
	v_cmp_lt_i32_e32 vcc, -1, v84
	s_and_saveexec_b64 s[34:35], vcc
	s_cbranch_execz .LBB1_216
	s_load_dwordx8 s[20:27], s[0:1], 0x8
	v_and_b32_e32 v69, 15, v0
	v_mov_b32_e32 v0, 0x8000
	v_lshrrev_b32_e32 v67, 4, v83
	v_lshl_or_b32 v88, v1, 10, v0
	s_mul_i32 s3, s2, 0x2710
	v_mul_u32_u24_e32 v0, 0x9c4, v1
	v_lshl_or_b32 v89, v69, 2, v67
	v_add3_u32 v90, s3, v0, v83
	v_lshlrev_b32_e32 v0, 2, v1
	v_mov_b32_e32 v2, 0x9000
	v_lshl_or_b32 v91, s2, 4, v0
	v_lshlrev_b32_e32 v0, 3, v89
	v_mov_b32_e32 v32, 0
	v_lshl_or_b32 v65, v1, 3, v2
	v_or_b32_e32 v2, 0x1e00, v0
	v_mov_b32_e32 v3, v32
	s_waitcnt lgkmcnt(0)
	v_lshl_add_u64 v[34:35], s[20:21], 0, v[2:3]
	v_or_b32_e32 v2, 0x1c00, v0
	v_lshl_add_u64 v[36:37], s[20:21], 0, v[2:3]
	v_or_b32_e32 v2, 0x1a00, v0
	v_lshl_add_u64 v[38:39], s[20:21], 0, v[2:3]
	v_or_b32_e32 v2, 0x1800, v0
	v_lshl_add_u64 v[40:41], s[20:21], 0, v[2:3]
	v_or_b32_e32 v2, 0x1600, v0
	v_lshl_add_u64 v[42:43], s[20:21], 0, v[2:3]
	v_or_b32_e32 v2, 0x1400, v0
	v_lshlrev_b32_e32 v63, 12, v1
	v_lshl_add_u64 v[44:45], s[20:21], 0, v[2:3]
	v_or_b32_e32 v2, 0x1200, v0
	v_mov_b32_e32 v1, v32
	v_lshl_or_b32 v71, v83, 3, v63
	v_lshl_or_b32 v73, v67, 3, v63
	v_lshl_add_u64 v[46:47], s[20:21], 0, v[2:3]
	v_or_b32_e32 v2, 0x1000, v0
	v_lshl_add_u64 v[50:51], s[20:21], 0, v[0:1]
	v_mbcnt_lo_u32_b32 v0, -1, 0
	v_or_b32_e32 v75, 4, v67
	v_or_b32_e32 v77, 8, v67
	v_or_b32_e32 v78, 12, v67
	v_or_b32_e32 v79, 16, v67
	v_or_b32_e32 v80, 20, v67
	v_or_b32_e32 v81, 24, v67
	v_or_b32_e32 v85, 28, v67
	v_or_b32_e32 v86, 64, v83
	v_or_b32_e32 v87, 0x4000, v63
	v_cmp_lt_u32_e64 s[0:1], 15, v83
	s_mul_i32 s39, s33, 0x9c4
	s_lshl_b32 s48, s33, 2
	v_or_b32_e32 v92, 0x200, v71
	v_or_b32_e32 v93, 0x204, v71
	v_or_b32_e32 v94, 0x100, v73
	v_lshl_add_u64 v[48:49], s[20:21], 0, v[2:3]
	s_mov_b32 s51, 0
	s_mov_b64 s[36:37], 0
	s_movk_i32 s49, 0x81
	s_mov_b32 s50, 0xff800000
	s_mov_b32 s38, 0x38d1b717
	v_mov_b32_e32 v95, 0xff800000
	v_mbcnt_hi_u32_b32 v96, -1, v0
	v_mov_b32_e32 v136, 0
	v_mov_b32_e32 v137, 0
	v_mov_b32_e32 v138, 0
	v_mov_b32_e32 v139, 0
	v_mov_b32_e32 v140, 0
	v_mov_b32_e32 v141, 0
	v_mov_b32_e32 v142, 0
	v_mov_b32_e32 v143, 0
	v_mov_b32_e32 v144, 0
	v_mov_b32_e32 v145, 0
	v_mov_b32_e32 v146, 0
	v_mov_b32_e32 v147, 0
	v_mov_b32_e32 v148, 0
	v_mov_b32_e32 v149, 0
	v_mov_b32_e32 v150, 0
	v_mov_b32_e32 v151, 0
	v_mov_b32_e32 v152, 0
	v_mov_b32_e32 v153, 0
	v_mov_b32_e32 v154, 0
	v_mov_b32_e32 v155, 0
	v_mov_b32_e32 v156, 0
	v_mov_b32_e32 v157, 0
	v_mov_b32_e32 v158, 0
	v_mov_b32_e32 v159, 0
	v_mov_b32_e32 v160, 0
	v_mov_b32_e32 v161, 0
	v_mov_b32_e32 v162, 0
	v_mov_b32_e32 v163, 0
	v_mov_b32_e32 v164, 0
	v_mov_b32_e32 v165, 0
	v_mov_b32_e32 v166, 0
	v_mov_b32_e32 v167, 0
	v_mov_b32_e32 v168, 0
	v_mov_b32_e32 v169, 0
	v_mov_b32_e32 v170, 0
	v_mov_b32_e32 v171, 0
	v_mov_b32_e32 v172, 0
	v_mov_b32_e32 v173, 0
	v_mov_b32_e32 v174, 0
	v_mov_b32_e32 v175, 0
	v_mov_b32_e32 v176, 0
	v_mov_b32_e32 v177, 0
	v_mov_b32_e32 v178, 0
	v_mov_b32_e32 v179, 0
	v_mov_b32_e32 v180, 0
	v_mov_b32_e32 v181, 0
	v_mov_b32_e32 v182, 0
	v_mov_b32_e32 v183, 0
	v_mov_b32_e32 v184, 0
	v_mov_b32_e32 v185, 0
	v_mov_b32_e32 v186, 0
	v_mov_b32_e32 v187, 0
	v_mov_b32_e32 v188, 0
	v_mov_b32_e32 v189, 0
	v_mov_b32_e32 v190, 0
	v_mov_b32_e32 v191, 0
	v_mov_b32_e32 v192, 0
	v_mov_b32_e32 v193, 0
	v_mov_b32_e32 v194, 0
	v_mov_b32_e32 v195, 0
	v_mov_b32_e32 v196, 0
	v_mov_b32_e32 v197, 0
	v_mov_b32_e32 v198, 0
	v_mov_b32_e32 v199, 0
	v_readfirstlane_b32 s54, v63
	s_lshr_b32 s54, s54, 12
	s_mul_i32 s4, s54, 0xfa
	s_and_b32 s56, s2, 7
	s_lshr_b32 s57, s2, 3
	s_mul_i32 s5, s56, 31
	s_min_u32 s56, s56, 2
	s_add_u32 s5, s5, s56
	s_add_u32 s5, s5, s57
	s_add_u32 s4, s4, s5
	v_mov_b32_e32 v82, s4
	v_mov_b32_e32 v87, 0x4000
	v_mov_b32_e32 v88, 0x8000
	v_mov_b32_e32 v65, 0x9030
	s_movk_i32 s3, 0x9c4
	v_mad_u32_u24 v90, v82, s3, v83
	v_lshlrev_b32_e32 v91, 2, v82
	s_branch .LBB1_9

.LBB1_217:
	s_andn2_saveexec_b64 s[0:1], s[30:31]
	s_cbranch_execz .LBB1_384
	v_readfirstlane_b32 s34, v1
	v_readfirstlane_b32 s36, v84
	v_and_b32_e32 v3, 63, v0
	v_lshlrev_b32_e32 v2, 4, v3
	s_cmp_lt_i32 s36, 0
	s_cbranch_scc1 .LBB1_384
	s_add_i32 s36, s36, 1
	s_lshl_b32 s36, s36, 2
	s_sub_i32 s36, s36, 1
	s_lshr_b32 s33, s33, 2
	s_mov_b32 s55, s34
	s_mul_i32 s43, s55, 0x2800
	s_and_b32 s56, s2, 7
	s_lshr_b32 s57, s2, 3
	s_mul_i32 s37, s56, 31
	s_min_u32 s56, s56, 2
	s_add_u32 s37, s37, s56
	s_add_u32 s37, s37, s57
	s_waitcnt lgkmcnt(0)
	s_and_b32 s29, s29, 0xffff
	s_mov_b32 s30, 0x17d78400
	s_mov_b32 s31, 0x20000
	s_mov_b32 s35, 0
	s_movk_i32 s7, 0x40
	s_mov_b32 s9, 0x7fffffff
	s_lshl_b32 s44, s34, 12
	s_add_u32 s44, s44, 0x4000
	s_lshl_b32 s45, s34, 10
	s_add_u32 s45, s45, 0x8000
	s_lshl_b32 s46, s34, 4
	s_add_u32 s46, s46, 0x9000
	s_and_b32 s47, s37, 1
	s_lshl_b32 s47, s47, 2
	s_mul_i32 s38, s37, 0x9c40
	s_lshl_b32 s40, s47, 4
	s_sub_u32 s38, s38, s40
	s_add_u32 s38, s38, s43
